# code placement: 48-byte pad before the MoE K-loop preheader
# speedup vs baseline: 1.0058x; 1.0058x over previous
.Lmoe_rows_direct:
	v_mov_b32_e32 v248, v134
	v_mov_b32_e32 v249, v136
	v_mov_b32_e32 v250, v138
	v_mov_b32_e32 v223, v140
	s_nop 0
	s_nop 0
	s_nop 0
	s_nop 0
	s_nop 0
	s_nop 0
	s_nop 0
	s_nop 0
	s_nop 0
	s_nop 0
	s_nop 0
	s_nop 0
